# conversion slots: even workgroups (3 slots) take 4 items per wave per slot, odd workgroups (4 slots) keep 3, so every wave converts 12 items inside the slots and the closing drain is empty
# baseline (speedup 1.0000x reference)
; #define LAS __attribute__((address_space(3)))
; DI kptr_t kargs_now() { kptr_t p = (kptr_t)__builtin_amdgcn_kernarg_segment_ptr(); asm volatile("" : "+s"(p)); return p; }
; #define RI_NEXT(D_) do { if (q.cnt == 8) { int b_ = 0; if (F.lane == 0) b_ = (int)__hip_atomic_fetch_add(qctr, 8u, __ATOMIC_RELAXED, __HIP_MEMORY_SCOPE_AGENT); q.base = __builtin_amdgcn_readfirstlane(b_); q.cnt = 0; } \
;         D_ = decode_item(KA, F.ws, kind, q.base + q.cnt); ++q.cnt; } while (0)
; DI void run_items1(Frame& F, int kind, int quota, QState& q) {
;     const kptr_t KA = kargs_now();
;     LAS float* scr = (LAS float*)(F.lds + F.wave * 16384);
;     unsigned* qctr = F.ctl + CW_QUEUE + 64 * kind;
;     ...
;     if (quota == 0) return;
;     TItem d; RI_NEXT(d); if (!d.valid) return;
; DI void phase_attn(Frame& F, int l) {
;     ...
;     QState cq; cq.base = 0; cq.cnt = 8;
;     constexpr int SLOT_ITEMS = 3;
;     if (F.bid & 1) { __syncthreads(); run_items1(F, 1 + l, SLOT_ITEMS, cq); }
.LBB0_398:
	v_readlane_b32 s8, v255, 14
	v_readlane_b32 s4, v253, 8
	s_lshl_b32 s58, s8, 6
	v_readlane_b32 s6, v253, 10
	v_readlane_b32 s7, v253, 11
	s_lshl_b64 s[0:1], s[58:59], 2
	s_mov_b64 s[2:3], s[6:7]
	s_add_u32 s0, s2, s0
	s_addc_u32 s1, s3, s1
	v_readlane_b32 s9, v255, 15
	s_add_u32 s12, s0, 0x8100
	s_addc_u32 s13, s1, 0
	v_readlane_b32 s100, v253, 29
	s_and_b32 s101, s100, 1
	s_xor_b32 s101, s101, 1
	s_add_i32 s101, s101, 2
	s_lshr_b32 s100, s100, 1
	s_and_b32 s100, s100, 15
	s_lshl_b32 s0, s100, 8
	s_mul_i32 s1, s8, 0xf00
	s_add_i32 s0, s0, s1
	s_add_i32 s0, s0, 0x1300
	s_add_u32 s12, s12, s0
	s_addc_u32 s13, s13, 0
	s_lshl_b64 s[0:1], s[8:9], 25
	v_writelane_b32 v255, s0, 16
	s_lshl_b64 s[62:63], s[8:9], 5
	s_lshl_b32 s2, s8, 20
	v_writelane_b32 v255, s1, 17
	s_mov_b32 s3, s59
	v_readlane_b32 s0, v253, 33
	v_writelane_b32 v255, s2, 18
	s_add_u32 s76, s0, s2
	v_readlane_b32 s0, v253, 34
	v_writelane_b32 v255, s3, 19
	s_addc_u32 s77, s0, 0
	s_lshl_b64 s[20:21], s[8:9], 21
	s_lshl_b64 s[0:1], s[8:9], 20
	v_readlane_b32 s2, v253, 35
	s_add_u32 s22, s2, s0
	v_readlane_b32 s2, v253, 36
	s_addc_u32 s23, s2, s1
	v_readlane_b32 s2, v253, 37
	s_add_u32 s24, s2, s0
	v_readlane_b32 s0, v253, 38
	s_addc_u32 s25, s0, s1
	s_lshl_b64 s[26:27], s[8:9], 24
	v_readlane_b32 s0, v253, 39
	s_add_u32 s14, s0, s44
	v_readlane_b32 s0, v253, 40
	s_addc_u32 s15, s0, s45
	s_mov_b32 s0, -1
	s_mov_b32 s95, 0
	v_mbcnt_lo_u32_b32 v0, s0, 0
	v_mbcnt_hi_u32_b32 v186, s0, v0
	v_readlane_b32 s0, v253, 29
	s_mov_b32 s51, s0
	s_mov_b64 s[30:31], s[70:71]
	s_bitcmp0_b32 s51, 0
	s_mov_b32 s63, 4
	v_readlane_b32 s5, v253, 9
	v_readlane_b32 s1, v253, 30
	s_cbranch_scc1 .LBB0_472
	s_mov_b64 s[6:7], s[70:71]
	v_mov_b32_e32 v0, 0
	v_cmp_eq_u32_e64 s[4:5], 0, v186
	s_waitcnt vmcnt(63) expcnt(7) lgkmcnt(15)
	s_barrier
	s_and_saveexec_b64 s[2:3], s[4:5]
	s_cbranch_execz .LBB0_403
	s_mov_b64 s[10:11], exec
	v_mbcnt_lo_u32_b32 v0, s10, 0
	v_mbcnt_hi_u32_b32 v0, s11, v0
	v_cmp_eq_u32_e32 vcc, 0, v0
	s_and_saveexec_b64 s[8:9], vcc
	s_cbranch_execz .LBB0_402
	s_bcnt1_i32_b64 s0, s[10:11]
	s_lshl_b32 s0, s0, 2
	v_mov_b32_e32 v2, s0
	global_atomic_add v2, v1, v2, s[12:13] sc0

; DI const float* inp(kptr_t k, int i) { return (const float*)k[i]; }
; DI int imap(int n, int H) { return ((n % H) / 128) * 256 + (n / H) * 128 + (n % 128); }
; DI TItem decode_item(kptr_t KA, unsigned char* ws, int kind, int it) {
;     TItem d; d.valid = it < (kind == 0 ? DEPTH * IT_SMALL : IT_EXP); if (!d.valid) it = 0;
;     const int l = kind == 0 ? it / IT_SMALL : kind - 1; int r = kind == 0 ? it % IT_SMALL : IT_SMALL + it;
;     const float* W; unsigned char* WT; int K, N, H = 0; bool f8 = false;
;     int nsub = 0, Kd = 0, kofs = 0;
;     if (r < IT_IN) { W = inp(KA, I_WIN) + (size_t)l * D * INW; K = D; N = INW;
;         WT = ws + WS_WIN + (size_t)l * INW * D; f8 = true; }
;     else if ((r -= IT_IN) < IT_GLU) { W = inp(KA, I_WGLU) + (size_t)l * SW * 1024; WT = ws + WS_WGLU + (size_t)l * 1024 * SW * 2; K = SW; N = 1024; H = 512; }
;     else if ((r -= IT_GLU) < IT_ATT) { W = inp(KA, I_WATTO) + (size_t)l * AW * D; WT = ws + WS_WCAT + (size_t)l * D * D; K = AW; N = D; Kd = D; f8 = true; }
;     else if ((r -= IT_ATT) < IT_SSMO) { W = inp(KA, I_WSSMO) + (size_t)l * SW * D; WT = ws + WS_WCAT + (size_t)l * D * D; K = SW; N = D; Kd = D; kofs = AW; f8 = true; }
;     else if ((r -= IT_SSMO) < IT_OUT) { W = inp(KA, I_WOUT) + (size_t)l * D * D; WT = ws + WS_WOUT + (size_t)l * D * D; K = D; N = D; f8 = true; }
;     else if ((r -= IT_OUT) < NE * IT_W1) { const int e = r / IT_W1; r %= IT_W1; W = inp(KA, I_WEXPIN) + ((size_t)l * NE + e) * D * 2048; WT = ws + WS_W1 + ((size_t)l * NE + e) * 2048 * D; K = D; N = 2048; H = 1024; f8 = true; }
;     else { r -= NE * IT_W1; const int e = r / IT_W2; r %= IT_W2; W = inp(KA, I_WEXPOUT) + ((size_t)l * NE + e) * DFF * D; WT = ws + WS_W2 + ((size_t)l * NE + e) * D * DFF; K = DFF; N = D; f8 = true; }
;     const int nblk = N / 64, kb = r / nblk, nb = r % nblk, n0 = nb * 64;
;     d.W = W; d.WT = WT; d.N = N; d.Kd = Kd ? Kd : K; d.kofs = kofs; d.drow0 = (H ? imap(n0, H) : n0) - nsub; d.k0 = kb * 64; d.n0 = n0; d.f8 = f8;
.LBB0_403:
	s_or_b64 exec, exec, s[2:3]
	v_readfirstlane_b32 s95, v0
	s_lshl_b32 s36, s95, 4
	s_or_b32 s36, s36, s100
	s_cmpk_lt_i32 s36, 0x6000
	s_cselect_b64 s[2:3], -1, 0
	s_and_b64 s[0:1], s[2:3], exec
	s_cselect_b32 s36, s36, 0
	s_add_i32 s0, s36, 0x680
	s_cmpk_gt_i32 s36, 0xfd7f
	s_mov_b64 s[18:19], -1
	s_cbranch_scc0 .LBB0_424
	s_mov_b64 s[34:35], -1
	s_cmpk_gt_u32 s0, 0x47f
	s_mov_b64 s[8:9], -1
	s_cbranch_scc0 .LBB0_421
	s_cmpk_gt_u32 s0, 0x4ff
	s_cbranch_scc0 .LBB0_418
	s_cmpk_gt_u32 s0, 0x57f
	s_cbranch_scc0 .LBB0_415
	s_cmp_lt_u32 s36, 0xfffff980
	s_cbranch_scc0 .LBB0_412
	s_mov_b64 s[28:29], -1
	s_cmpk_gt_u32 s0, 0x467f
	s_cbranch_scc0 .LBB0_410
	s_add_i32 s1, s36, 0xffffc000
	s_lshr_b32 s58, s1, 8
	s_load_dwordx2 s[8:9], s[6:7], 0xd0
	s_and_b32 s1, s36, 0xff
	s_lshl_b64 s[10:11], s[58:59], 20
	v_readlane_b32 s16, v255, 16
	v_readlane_b32 s17, v255, 17
	s_add_u32 s10, s10, s16
	s_addc_u32 s11, s11, s17
	s_lshl_b64 s[16:17], s[10:11], 2
	s_waitcnt lgkmcnt(0)
	s_add_u32 s16, s8, s16
	s_addc_u32 s17, s9, s17
	v_readlane_b32 s8, v253, 45
	s_add_u32 s10, s8, s10
	v_readlane_b32 s8, v253, 46
	s_addc_u32 s11, s8, s11
	s_mov_b64 s[8:9], 0

; #define LAS __attribute__((address_space(3)))
; #define LDS_WAIT() asm volatile("s_waitcnt lgkmcnt(0)" ::: "memory")
; #define RI_NEXT(D_) do { if (q.cnt == 8) { int b_ = 0; if (F.lane == 0) b_ = (int)__hip_atomic_fetch_add(qctr, 8u, __ATOMIC_RELAXED, __HIP_MEMORY_SCOPE_AGENT); q.base = __builtin_amdgcn_readfirstlane(b_); q.cnt = 0; } \
;         D_ = decode_item(KA, F.ws, kind, q.base + q.cnt); ++q.cnt; } while (0)
; DI void item_scatter(const f32x4 (&v)[16], LAS float* scr, int lane) {
;     const int r4 = lane >> 4, c4 = lane & 15;
; #pragma unroll
;     for (int i = 0; i < 16; ++i) { const int k = 4 * i + r4;
; #pragma unroll
;         for (int j = 0; j < 4; ++j) scr[(4 * c4 + j) * 64 + (k ^ (4 * (c4 ^ j)))] = v[i][j]; }
;     LDS_WAIT(); asm volatile("" ::: "memory");
; }
; DI void run_items1(Frame& F, int kind, int quota, QState& q) {
;     ...
;     for (int n = 1; ; ++n) {
;         item_scatter(v, scr, F.lane);
;         TItem dn; dn.valid = false;
;         if (quota < 0 || n < quota) { RI_NEXT(dn); if (dn.valid) item_load(dn, v, F.lane); }
.LBB0_602:
	s_waitcnt vmcnt(15)
	ds_write_b32 v93, v2
	ds_write_b32 v94, v3 offset:256
	ds_write_b32 v95, v4 offset:512
	ds_write_b32 v96, v5 offset:768
	s_waitcnt vmcnt(14)
	ds_write_b32 v97, v6
	ds_write_b32 v98, v7 offset:256
	ds_write_b32 v99, v8 offset:512
	ds_write_b32 v100, v9 offset:768
	s_waitcnt vmcnt(13)
	ds_write_b32 v101, v10
	ds_write_b32 v102, v11 offset:256
	ds_write_b32 v103, v12 offset:512
	ds_write_b32 v104, v13 offset:768
	s_waitcnt vmcnt(12)
	ds_write_b32 v105, v14
	ds_write_b32 v106, v15 offset:256
	ds_write_b32 v107, v16 offset:512
	ds_write_b32 v108, v17 offset:768
	s_waitcnt vmcnt(11)
	ds_write_b32 v109, v18
	ds_write_b32 v110, v19 offset:256
	ds_write_b32 v111, v20 offset:512
	ds_write_b32 v112, v21 offset:768
	s_waitcnt vmcnt(10)
	ds_write_b32 v113, v22
	ds_write_b32 v114, v23 offset:256
	ds_write_b32 v115, v24 offset:512
	ds_write_b32 v116, v25 offset:768
	s_waitcnt vmcnt(9)
	ds_write_b32 v117, v26
	ds_write_b32 v118, v27 offset:256
	ds_write_b32 v119, v28 offset:512
	ds_write_b32 v120, v29 offset:768
	s_waitcnt vmcnt(8)
	ds_write_b32 v121, v30
	ds_write_b32 v122, v31 offset:256
	ds_write_b32 v123, v32 offset:512
	ds_write_b32 v124, v33 offset:768
	s_waitcnt vmcnt(7)
	ds_write_b32 v125, v34
	ds_write_b32 v126, v35 offset:256
	ds_write_b32 v127, v36 offset:512
	ds_write_b32 v128, v37 offset:768
	s_waitcnt vmcnt(6)
	ds_write_b32 v129, v38
	ds_write_b32 v130, v39 offset:256
	ds_write_b32 v131, v40 offset:512
	ds_write_b32 v132, v41 offset:768
	s_waitcnt vmcnt(5)
	ds_write_b32 v133, v42
	ds_write_b32 v134, v43 offset:256
	ds_write_b32 v135, v44 offset:512
	ds_write_b32 v136, v45 offset:768
	s_waitcnt vmcnt(4)
	ds_write_b32 v137, v46
	ds_write_b32 v138, v47 offset:256
	ds_write_b32 v139, v48 offset:512
	ds_write_b32 v140, v49 offset:768
	s_waitcnt vmcnt(3)
	ds_write_b32 v141, v50
	ds_write_b32 v142, v51 offset:256
	ds_write_b32 v143, v52 offset:512
	ds_write_b32 v144, v53 offset:768
	s_waitcnt vmcnt(2)
	ds_write_b32 v145, v54
	ds_write_b32 v146, v55 offset:256
	ds_write_b32 v147, v56 offset:512
	ds_write_b32 v148, v57 offset:768
	s_waitcnt vmcnt(1)
	ds_write_b32 v149, v58
	ds_write_b32 v150, v59 offset:256
	ds_write_b32 v151, v60 offset:512
	ds_write_b32 v152, v61 offset:768
	s_waitcnt vmcnt(0)
	ds_write_b32 v153, v62
	ds_write_b32 v154, v63 offset:256
	ds_write_b32 v155, v64 offset:512
	ds_write_b32 v156, v65 offset:768
	s_waitcnt lgkmcnt(0)
	s_cmp_gt_u32 s38, s101
	s_mov_b64 s[2:3], 0
	s_cbranch_scc1 .LBB0_637
	s_cmp_lg_u32 s63, 4
	s_cbranch_scc1 .LBB0_609
	v_mov_b32_e32 v0, 0
	s_and_saveexec_b64 s[2:3], s[4:5]
	s_cbranch_execz .LBB0_608
	s_mov_b64 s[18:19], exec
	v_mbcnt_lo_u32_b32 v0, s18, 0
	v_mbcnt_hi_u32_b32 v0, s19, v0
	v_cmp_eq_u32_e32 vcc, 0, v0
	s_and_saveexec_b64 s[16:17], vcc
	s_cbranch_execz .LBB0_607
	s_bcnt1_i32_b64 s0, s[18:19]
	s_lshl_b32 s0, s0, 2
	v_mov_b32_e32 v66, s0
	global_atomic_add v66, v1, v66, s[12:13] sc0
